# layer-0 prologue: input-weight and bias loads issued unmasked up front with one wait (was 8 serialized drains), on robust base
# speedup vs baseline: 1.0125x; 1.0125x over previous
.LBB1_400:
	s_andn2_b64 vcc, exec, s[6:7]
	s_cbranch_vccnz .LBB1_434
	v_lshlrev_b32_e32 v34, 4, v0
	v_mov_b32_e32 v35, 0
	v_lshl_add_u64 v[2:3], s[28:29], 0, v[34:35]
	v_add_co_u32_e32 v4, vcc, 0x3000, v2
	s_load_dwordx8 s[4:11], s[0:1], 0x8
	s_nop 0
	v_addc_co_u32_e32 v5, vcc, 0, v3, vcc
	v_add_co_u32_e32 v6, vcc, 0x6000, v2
	v_or_b32_e32 v107, 0xc00, v0
	s_nop 0
	v_addc_co_u32_e32 v7, vcc, 0, v3, vcc
	v_add_co_u32_e32 v2, vcc, 0x9000, v2
	global_load_dwordx4 v[68:71], v34, s[28:29]
	s_nop 0
	v_addc_co_u32_e32 v3, vcc, 0, v3, vcc
	global_load_dwordx4 v[30:33], v[4:5], off
	global_load_dwordx4 v[26:29], v[6:7], off
	v_lshlrev_b32_e32 v4, 4, v107
	global_load_dwordx4 v[22:25], v[2:3], off
	global_load_dwordx4 v[18:21], v4, s[28:29]
	v_and_b32_e32 v6, 3, v0
	v_bfe_u32 v2, v0, 2, 2
	v_lshl_or_b32 v2, v6, 6, v2
	v_lshl_or_b32 v14, s68, 4, v2
	v_lshrrev_b32_e32 v1, 4, v106
	v_mov_b32_e32 v2, 0xbfb8aa3b
	v_mov_b32_e32 v3, 0xc038aa3b
	v_cmp_eq_u32_e32 vcc, 2, v6
	v_cmp_gt_u32_e64 s[2:3], 16, v106
	v_lshlrev_b32_e32 v108, 5, v14
	v_cndmask_b32_e32 v104, v2, v3, vcc
	v_lshlrev_b32_e32 v109, 2, v14
	v_lshlrev_b32_e32 v110, 8, v14
	v_mov_b32_e32 v105, v104
	v_lshl_add_u32 v110, v1, 5, v110
	s_waitcnt lgkmcnt(0)
	global_load_dwordx4 v[36:39], v108, s[4:5]
	global_load_dwordx4 v[40:43], v108, s[4:5] offset:16
	global_load_dwordx4 v[44:47], v108, s[4:5] offset:128
	global_load_dwordx4 v[48:51], v108, s[4:5] offset:144
	global_load_dwordx4 v[52:55], v108, s[4:5] offset:256
	global_load_dwordx4 v[56:59], v108, s[4:5] offset:272
	global_load_dwordx4 v[60:63], v108, s[4:5] offset:384
	global_load_dwordx4 v[64:67], v108, s[4:5] offset:400
	global_load_dword v72, v109, s[8:9]
	global_load_dword v76, v109, s[10:11]
	global_load_dword v73, v109, s[8:9] offset:16
	global_load_dword v77, v109, s[10:11] offset:16
	global_load_dword v74, v109, s[8:9] offset:32
	global_load_dword v78, v109, s[10:11] offset:32
	global_load_dword v75, v109, s[8:9] offset:48
	global_load_dword v79, v109, s[10:11] offset:48
	v_mov_b32_e32 v2, 0
	v_mov_b32_e32 v3, 0
	v_mov_b32_e32 v4, 0
	v_mov_b32_e32 v5, 0
	v_mov_b32_e32 v6, 0
	v_mov_b32_e32 v7, 0
	v_mov_b32_e32 v8, 0
	v_mov_b32_e32 v9, 0
	v_mov_b32_e32 v10, 0
	v_mov_b32_e32 v11, 0
	v_mov_b32_e32 v12, 0
	v_mov_b32_e32 v13, 0
	v_mov_b32_e32 v14, 0
	v_mov_b32_e32 v15, 0
	v_mov_b32_e32 v16, 0
	v_mov_b32_e32 v17, 0
	s_waitcnt vmcnt(0)
	s_and_saveexec_b64 s[12:13], s[2:3]
	v_fma_mixlo_f16 v111, v104, v36, 0
	v_mul_f32_e32 v37, v104, v37
	v_mul_f32_e32 v38, v104, v38
	v_mul_f32_e32 v39, v104, v39
	v_mul_f32_e32 v40, v104, v40
	v_mul_f32_e32 v41, v104, v41
	v_mul_f32_e32 v42, v104, v42
	v_cvt_pk_f16_f32 v37, v37, v38
	v_cvt_pk_f16_f32 v39, v39, v40
	v_cvt_pk_f16_f32 v41, v41, v42
	v_pack_b32_f16 v2, v111, v37
	v_alignbit_b32 v3, v39, v37, 16
	v_alignbit_b32 v4, v41, v39, 16
	v_lshrrev_b32_e32 v5, 16, v41
	v_fma_mixhi_f16 v5, v104, v43, 0
	v_fma_mixlo_f16 v111, v104, v44, 0
	v_mul_f32_e32 v45, v104, v45
	v_mul_f32_e32 v46, v104, v46
	v_mul_f32_e32 v47, v104, v47
	v_mul_f32_e32 v48, v104, v48
	v_mul_f32_e32 v49, v104, v49
	v_mul_f32_e32 v50, v104, v50
	v_cvt_pk_f16_f32 v45, v45, v46
	v_cvt_pk_f16_f32 v47, v47, v48
	v_cvt_pk_f16_f32 v49, v49, v50
	v_pack_b32_f16 v6, v111, v45
	v_alignbit_b32 v7, v47, v45, 16
	v_alignbit_b32 v8, v49, v47, 16
	v_lshrrev_b32_e32 v9, 16, v49
	v_fma_mixhi_f16 v9, v104, v51, 0
	v_fma_mixlo_f16 v111, v104, v52, 0
	v_mul_f32_e32 v53, v104, v53
	v_mul_f32_e32 v54, v104, v54
	v_mul_f32_e32 v55, v104, v55
	v_mul_f32_e32 v56, v104, v56
	v_mul_f32_e32 v57, v104, v57
	v_mul_f32_e32 v58, v104, v58
	v_cvt_pk_f16_f32 v53, v53, v54
	v_cvt_pk_f16_f32 v55, v55, v56
	v_cvt_pk_f16_f32 v57, v57, v58
	v_pack_b32_f16 v10, v111, v53
	v_alignbit_b32 v11, v55, v53, 16
	v_alignbit_b32 v12, v57, v55, 16
	v_lshrrev_b32_e32 v13, 16, v57
	v_fma_mixhi_f16 v13, v104, v59, 0
	v_fma_mixlo_f16 v111, v104, v60, 0
	v_mul_f32_e32 v61, v104, v61
	v_mul_f32_e32 v62, v104, v62
	v_mul_f32_e32 v63, v104, v63
	v_mul_f32_e32 v64, v104, v64
	v_mul_f32_e32 v65, v104, v65
	v_mul_f32_e32 v66, v104, v66
	v_cvt_pk_f16_f32 v61, v61, v62
	v_cvt_pk_f16_f32 v63, v63, v64
	v_cvt_pk_f16_f32 v65, v65, v66
	v_pack_b32_f16 v14, v111, v61
	v_alignbit_b32 v15, v63, v61, 16
	v_alignbit_b32 v16, v65, v63, 16
	v_lshrrev_b32_e32 v17, 16, v65
	v_fma_mixhi_f16 v17, v104, v67, 0
	s_mov_b64 exec, s[12:13]
	v_cmp_eq_u32_e32 vcc, 1, v1
	s_mov_b32 s14, 0xffff
	s_and_saveexec_b64 s[12:13], vcc
	v_add_f32_e32 v111, v72, v76
	v_fma_mixlo_f16 v111, v104, v111, 0
	v_bfi_b32 v2, s14, v111, v2
	v_add_f32_e32 v111, v73, v77
	v_fma_mixlo_f16 v111, v104, v111, 0
	v_bfi_b32 v6, s14, v111, v6
	v_add_f32_e32 v111, v74, v78
	v_fma_mixlo_f16 v111, v104, v111, 0
	v_bfi_b32 v10, s14, v111, v10
	v_add_f32_e32 v111, v75, v79
	v_fma_mixlo_f16 v111, v104, v111, 0
	v_bfi_b32 v14, s14, v111, v14
	s_mov_b64 exec, s[12:13]
	global_load_dwordx4 v[44:47], v110, s[6:7] offset:16
	global_load_dwordx4 v[56:59], v110, s[6:7]
	global_load_dwordx4 v[48:51], v110, s[6:7] offset:144
	global_load_dwordx4 v[52:55], v110, s[6:7] offset:128
	global_load_dwordx4 v[36:39], v110, s[6:7] offset:1040
	global_load_dwordx4 v[64:67], v110, s[6:7] offset:1024
	global_load_dwordx4 v[40:43], v110, s[6:7] offset:1168
	global_load_dwordx4 v[60:63], v110, s[6:7] offset:1152
	global_load_dwordx4 v[80:83], v110, s[6:7] offset:2064
	global_load_dwordx4 v[84:87], v110, s[6:7] offset:2048
	global_load_dwordx4 v[72:75], v110, s[6:7] offset:2192
	global_load_dwordx4 v[76:79], v110, s[6:7] offset:2176
	global_load_dwordx4 v[96:99], v110, s[6:7] offset:3088
	global_load_dwordx4 v[100:103], v110, s[6:7] offset:3072
	global_load_dwordx4 v[88:91], v110, s[6:7] offset:3216
	global_load_dwordx4 v[92:95], v110, s[6:7] offset:3200
	v_mul_u32_u24_e32 v110, 0x556, v0
	v_lshrrev_b32_e32 v110, 16, v110
	v_mul_lo_u16_e32 v111, 48, v110
	v_sub_u16_e32 v111, v0, v111
	v_lshrrev_b32_e32 v112, 1, v111
	s_waitcnt vmcnt(20)
	v_cvt_pk_f16_f32 v71, v70, v71
	v_cvt_pk_f16_f32 v70, v68, v69
	s_movk_i32 s4, 0x50
	v_lshlrev_b32_e32 v69, 3, v111
	v_mad_u32_u24 v68, v112, s4, v110
	v_and_b32_e32 v69, 8, v69
	v_lshl_or_b32 v68, v68, 4, v69
	v_add_u32_e32 v35, 0x300, v0
	v_add_u32_e32 v68, 0x14000, v68
	ds_write_b64 v68, v[70:71]
	v_mul_u32_u24_e32 v68, 0x556, v35
	v_lshrrev_b32_e32 v68, 16, v68
	v_mul_lo_u16_e32 v69, 48, v68
	v_sub_u16_e32 v35, v35, v69
	v_lshrrev_b32_e32 v69, 1, v35
	s_waitcnt vmcnt(19)
	v_cvt_pk_f16_f32 v33, v32, v33
	v_cvt_pk_f16_f32 v32, v30, v31
	v_lshlrev_b32_e32 v31, 3, v35
	v_mad_u32_u24 v30, v69, s4, v68
	v_and_b32_e32 v31, 8, v31
	v_lshl_or_b32 v30, v30, 4, v31
	v_add_u32_e32 v108, 0x600, v0
	v_add_u32_e32 v30, 0x14000, v30
	ds_write_b64 v30, v[32:33]
	v_mul_u32_u24_e32 v30, 0xaab, v108
	v_lshrrev_b32_e32 v30, 17, v30
	v_mul_lo_u16_e32 v31, 48, v30
	v_sub_u16_e32 v31, v108, v31
	v_lshrrev_b32_e32 v32, 1, v31
	s_waitcnt vmcnt(18)
	v_cvt_pk_f16_f32 v29, v28, v29
	v_cvt_pk_f16_f32 v28, v26, v27
	v_lshlrev_b32_e32 v27, 3, v31
	v_mad_u32_u24 v26, v32, s4, v30
	v_and_b32_e32 v27, 8, v27
	v_lshl_or_b32 v26, v26, 4, v27
	v_add_u32_e32 v109, 0x900, v0
	v_add_u32_e32 v26, 0x14000, v26
	ds_write_b64 v26, v[28:29]
	v_mul_u32_u24_e32 v26, 0xaab, v109
	v_lshrrev_b32_e32 v26, 17, v26
	v_mul_lo_u16_e32 v27, 48, v26
	v_sub_u16_e32 v27, v109, v27
	v_lshrrev_b32_e32 v28, 1, v27
	s_waitcnt vmcnt(17)
	v_cvt_pk_f16_f32 v25, v24, v25
	v_cvt_pk_f16_f32 v24, v22, v23
	v_lshlrev_b32_e32 v23, 3, v27
	v_mad_u32_u24 v22, v28, s4, v26
	v_and_b32_e32 v23, 8, v23
	v_lshl_or_b32 v22, v22, 4, v23
	v_add_u32_e32 v22, 0x14000, v22
	ds_write_b64 v22, v[24:25]
	v_mul_u32_u24_e32 v22, 0xaab, v107
	v_lshrrev_b32_e32 v22, 17, v22
	v_mul_lo_u16_e32 v23, 48, v22
	v_sub_u16_e32 v23, v107, v23
	v_lshrrev_b32_e32 v24, 1, v23
	s_waitcnt vmcnt(16)
	v_cvt_pk_f16_f32 v21, v20, v21
	v_cvt_pk_f16_f32 v20, v18, v19
	v_lshlrev_b32_e32 v19, 3, v23
	v_mad_u32_u24 v18, v24, s4, v22
	v_and_b32_e32 v19, 8, v19
	v_lshl_or_b32 v18, v18, 4, v19
	s_movk_i32 s4, 0x9f
	v_add_u32_e32 v18, 0x14000, v18
	v_cmp_lt_u32_e64 s[4:5], s4, v0
	ds_write_b64 v18, v[20:21]
	s_and_saveexec_b64 s[6:7], s[4:5]
	s_xor_b64 s[4:5], exec, s[6:7]
	v_lshlrev_b32_e32 v34, 4, v0
	s_andn2_saveexec_b64 s[6:7], s[4:5]
	s_cbranch_execz .LBB1_421
	s_movk_i32 s4, 0x50
	v_mov_b32_e32 v18, 0x3c00
	v_cmp_gt_u32_e64 s[4:5], s4, v0
	v_mov_b32_e32 v19, 0
	v_add_u32_e32 v22, 0x1b800, v34
	v_cndmask_b32_e64 v18, 0, v18, s[4:5]
	v_mov_b32_e32 v20, v19
	v_mov_b32_e32 v21, v19
	ds_write_b128 v22, v[18:21]
